# P11 rope epilogue: rotary table values of all 8 row groups preloaded once into dead fragment registers (14 loads in flight, one wait) instead of a load+wait per group behind the previous stores
# speedup vs baseline: 1.0522x; 1.0003x over previous
; DI unsigned pk_bf16(float lo, float hi) { f32x2 v = {lo, hi}; hbf16x2 r = __builtin_convertvector(v, hbf16x2); return __builtin_bit_cast(unsigned, r); }
;     DI void operator()(const f32x4 (&acc)[2][2][4][2], const pg8::GU& u, int wr, int wc, int fr, int fq) const {
;     ...
;             const int col0 = 32 * g32 + 4 * fq;
; #pragma unroll
;             for (int ai = 0; ai < 2; ++ai)
; #pragma unroll
;                 for (int m = 0; m < 4; ++m) {
;                     const int row = row0 + ai * 128 + m * 16;
;                     f32x4 x1 = acc[ai][bj][m][0], x2 = acc[ai][bj][m][1];
;                     if (MODE == 0) { x1 *= 0.07216878364870322f * LOG2E; x2 *= 0.07216878364870322f * LOG2E; }
;                     if (rot && row >= NCTX) {
;                         const int t = (row - NCTX) & (SEQ - 1), pos = axis ? (t & 63) : (t >> 6);
;                         const f32x2* cs = R + pos * (MODE == 0 ? 16 : 32) + ibase;
;                         f32x4 o1, o2;
; #pragma unroll
;                         for (int j = 0; j < 4; ++j) { const f32x2 c = cs[j]; o1[j] = x1[j] * c[0] - x2[j] * c[1]; o2[j] = x2[j] * c[0] + x1[j] * c[1]; }
;                         x1 = o1; x2 = o2;
;                     }
;                     bf16_t* rowp = O + (size_t)row * ldc + col0;
;                     u32x2 w1, w2; w1.x = pk_bf16(x1[0], x1[1]); w1.y = pk_bf16(x1[2], x1[3]); w2.x = pk_bf16(x2[0], x2[1]); w2.y = pk_bf16(x2[2], x2[3]);
;                     *(u32x2*)(rowp) = w1; *(u32x2*)(rowp + 16) = w2;
;                 }
.LBB0_1207:
	s_lshl_b32 s15, s34, 8
	s_add_i32 s15, s15, s81
	s_nop 15
	s_nop 15
	v_or_b32_e32 v24, s15, v185
	s_cmp_lt_i32 s30, 5
	s_cselect_b64 s[66:67], -1, 0
	s_bfe_u32 s15, s15, 0x50006
	v_cmp_lt_i32_e32 vcc, s87, v24
	s_xor_b32 s15, s15, 16
	s_and_b64 s[34:35], s[66:67], vcc
	s_cmp_eq_u64 s[66:67], 0
	s_cbranch_scc1 .Lrope11_nopre
	v_add_u32_e32 v248, 0x80, v24
	v_lshrrev_b32_e32 v248, 6, v248
	v_bitop3_b32 v248, v248, 16, 31 bitop3:0x6c
	v_mov_b32_e32 v249, s15
	v_cndmask_b32_e64 v249, v186, v249, s[2:3]
	v_lshlrev_b32_e32 v166, 8, v249
	v_lshl_add_u64 v[176:177], v[168:169], 0, v[166:167]
	global_load_dwordx4 v[180:183], v[176:177], off offset:16
	global_load_dwordx4 v[176:179], v[176:177], off
	v_mov_b32_e32 v249, s15
	v_cndmask_b32_e64 v249, v187, v249, s[2:3]
	v_lshlrev_b32_e32 v166, 8, v249
	v_lshl_add_u64 v[196:197], v[168:169], 0, v[166:167]
	global_load_dwordx4 v[200:203], v[196:197], off offset:16
	global_load_dwordx4 v[196:199], v[196:197], off
	v_mov_b32_e32 v249, s15
	v_cndmask_b32_e64 v249, v188, v249, s[2:3]
	v_lshlrev_b32_e32 v166, 8, v249
	v_lshl_add_u64 v[204:205], v[168:169], 0, v[166:167]
	global_load_dwordx4 v[208:211], v[204:205], off offset:16
	global_load_dwordx4 v[204:207], v[204:205], off
	v_mov_b32_e32 v249, v248
	v_cndmask_b32_e64 v249, v185, v249, s[2:3]
	v_lshlrev_b32_e32 v166, 8, v249
	v_lshl_add_u64 v[212:213], v[168:169], 0, v[166:167]
	global_load_dwordx4 v[216:219], v[212:213], off offset:16
	global_load_dwordx4 v[212:215], v[212:213], off
	v_mov_b32_e32 v249, v248
	v_cndmask_b32_e64 v249, v186, v249, s[2:3]
	v_lshlrev_b32_e32 v166, 8, v249
	v_lshl_add_u64 v[224:225], v[168:169], 0, v[166:167]
	global_load_dwordx4 v[228:231], v[224:225], off offset:16
	global_load_dwordx4 v[224:227], v[224:225], off
	v_mov_b32_e32 v249, v248
	v_cndmask_b32_e64 v249, v187, v249, s[2:3]
	v_lshlrev_b32_e32 v166, 8, v249
	v_lshl_add_u64 v[232:233], v[168:169], 0, v[166:167]
	global_load_dwordx4 v[236:239], v[232:233], off offset:16
	global_load_dwordx4 v[232:235], v[232:233], off
	v_mov_b32_e32 v249, v248
	v_cndmask_b32_e64 v249, v188, v249, s[2:3]
	v_lshlrev_b32_e32 v166, 8, v249
	v_lshl_add_u64 v[240:241], v[168:169], 0, v[166:167]
	global_load_dwordx4 v[244:247], v[240:241], off offset:16
	global_load_dwordx4 v[240:243], v[240:241], off
.Lrope11_nopre:
	s_and_saveexec_b64 s[40:41], s[34:35]
	s_cbranch_execz .LBB0_1209
	v_mov_b32_e32 v2, s15
	v_cndmask_b32_e64 v2, v185, v2, s[2:3]
	v_lshlrev_b32_e32 v166, 8, v2
	v_lshl_add_u64 v[6:7], v[168:169], 0, v[166:167]
	global_load_dwordx4 v[2:5], v[6:7], off
	s_nop 0
	global_load_dwordx4 v[6:9], v[6:7], off offset:16
	s_waitcnt vmcnt(0)
	v_mov_b32_e32 v10, v2
	v_mul_f32_e32 v2, v160, v6
	v_mul_f32_e32 v12, v156, v7
	v_mul_f32_e32 v6, v156, v6
	v_mov_b32_e32 v156, v161
	v_mul_f32_e32 v14, v160, v7
	v_mov_b32_e32 v160, v157
	v_pk_mul_f32 v[18:19], v[156:157], v[8:9]
	v_mov_b32_e32 v11, v4
	v_mov_b32_e32 v4, v3
	v_pk_mul_f32 v[8:9], v[160:161], v[8:9]
	v_mov_b32_e32 v3, v18
	v_mov_b32_e32 v13, v19
	v_pk_mul_f32 v[16:17], v[154:155], v[4:5]
	v_pk_mul_f32 v[4:5], v[158:159], v[4:5]
	v_mov_b32_e32 v7, v8
	v_mov_b32_e32 v15, v9
	v_pk_add_f32 v[2:3], v[2:3], v[12:13] neg_lo:[0,1] neg_hi:[0,1]
	v_pk_fma_f32 v[158:159], v[158:159], v[10:11], v[16:17] neg_lo:[0,0,1] neg_hi:[0,0,1]
	v_pk_fma_f32 v[154:155], v[154:155], v[10:11], v[4:5]
	v_pk_add_f32 v[156:157], v[6:7], v[14:15]
	v_mov_b32_e32 v160, v2
	v_mov_b32_e32 v161, v3
.LBB0_1209:
	s_or_b64 exec, exec, s[40:41]
	v_lshl_or_b32 v22, s30, 8, v190
	v_mov_b64_e32 v[2:3], s[4:5]
	v_ashrrev_i32_e32 v23, 31, v22
	v_mad_i64_i32 v[2:3], s[30:31], v24, s88, v[2:3]
	v_lshl_add_u64 v[2:3], v[22:23], 1, v[2:3]
	v_cvt_pk_bf16_f32 v4, v158, v159
	v_cvt_pk_bf16_f32 v5, v160, v161
	v_cvt_pk_bf16_f32 v6, v154, v155
	v_cvt_pk_bf16_f32 v7, v156, v157
	global_store_dwordx2 v[2:3], v[4:5], off
	global_store_dwordx2 v[2:3], v[6:7], off offset:32
	v_or_b32_e32 v4, 16, v24
	v_cmp_lt_i32_e32 vcc, s87, v4
	s_and_b64 s[30:31], s[66:67], vcc
	s_and_saveexec_b64 s[40:41], s[30:31]
	s_cbranch_execz .LBB0_1211
	v_mov_b32_e32 v5, s15
	v_cndmask_b32_e64 v5, v186, v5, s[2:3]
	v_lshlrev_b32_e32 v166, 8, v5
	v_lshl_add_u64 v[10:11], v[168:169], 0, v[166:167]
	v_mov_b32_e32 v14, v176
	v_mul_f32_e32 v6, v152, v180
	v_mul_f32_e32 v16, v148, v181
	v_mul_f32_e32 v10, v148, v180
	v_mov_b32_e32 v148, v153
	v_mul_f32_e32 v18, v152, v181
	v_mov_b32_e32 v152, v149
	v_pk_mul_f32 v[26:27], v[148:149], v[182:183]
	v_mov_b32_e32 v15, v178
	v_mov_b32_e32 v8, v177
	v_pk_mul_f32 v[12:13], v[152:153], v[182:183]
	v_mov_b32_e32 v7, v26
	v_mov_b32_e32 v17, v27
	v_mov_b32_e32 v9, v179
	v_pk_mul_f32 v[20:21], v[146:147], v[8:9]
	v_pk_mul_f32 v[8:9], v[150:151], v[8:9]
	v_mov_b32_e32 v11, v12
	v_mov_b32_e32 v19, v13
	v_pk_add_f32 v[6:7], v[6:7], v[16:17] neg_lo:[0,1] neg_hi:[0,1]
	v_pk_fma_f32 v[150:151], v[150:151], v[14:15], v[20:21] neg_lo:[0,0,1] neg_hi:[0,0,1]
	v_pk_fma_f32 v[146:147], v[146:147], v[14:15], v[8:9]
	v_pk_add_f32 v[148:149], v[10:11], v[18:19]
	v_mov_b32_e32 v152, v6
	v_mov_b32_e32 v153, v7
; DI unsigned pk_bf16(float lo, float hi) { f32x2 v = {lo, hi}; hbf16x2 r = __builtin_convertvector(v, hbf16x2); return __builtin_bit_cast(unsigned, r); }
;     DI void operator()(const f32x4 (&acc)[2][2][4][2], const pg8::GU& u, int wr, int wc, int fr, int fq) const {
;     ...
;             const int col0 = 32 * g32 + 4 * fq;
; #pragma unroll
;             for (int ai = 0; ai < 2; ++ai)
; #pragma unroll
;                 for (int m = 0; m < 4; ++m) {
;                     const int row = row0 + ai * 128 + m * 16;
;                     f32x4 x1 = acc[ai][bj][m][0], x2 = acc[ai][bj][m][1];
;                     if (MODE == 0) { x1 *= 0.07216878364870322f * LOG2E; x2 *= 0.07216878364870322f * LOG2E; }
;                     if (rot && row >= NCTX) {
;                         const int t = (row - NCTX) & (SEQ - 1), pos = axis ? (t & 63) : (t >> 6);
;                         const f32x2* cs = R + pos * (MODE == 0 ? 16 : 32) + ibase;
;                         f32x4 o1, o2;
; #pragma unroll
;                         for (int j = 0; j < 4; ++j) { const f32x2 c = cs[j]; o1[j] = x1[j] * c[0] - x2[j] * c[1]; o2[j] = x2[j] * c[0] + x1[j] * c[1]; }
;                         x1 = o1; x2 = o2;
;                     }
;                     bf16_t* rowp = O + (size_t)row * ldc + col0;
;                     u32x2 w1, w2; w1.x = pk_bf16(x1[0], x1[1]); w1.y = pk_bf16(x1[2], x1[3]); w2.x = pk_bf16(x2[0], x2[1]); w2.y = pk_bf16(x2[2], x2[3]);
;                     *(u32x2*)(rowp) = w1; *(u32x2*)(rowp + 16) = w2;
;                 }
.LBB0_1211:
	s_or_b64 exec, exec, s[40:41]
	v_mov_b64_e32 v[6:7], s[4:5]
	v_mad_i64_i32 v[4:5], s[40:41], v4, s88, v[6:7]
	v_lshl_add_u64 v[4:5], v[22:23], 1, v[4:5]
	v_cvt_pk_bf16_f32 v6, v150, v151
	v_cvt_pk_bf16_f32 v7, v152, v153
	v_cvt_pk_bf16_f32 v8, v146, v147
	v_cvt_pk_bf16_f32 v9, v148, v149
	global_store_dwordx2 v[4:5], v[6:7], off
	global_store_dwordx2 v[4:5], v[8:9], off offset:32
	v_or_b32_e32 v6, 32, v24
	v_cmp_lt_i32_e32 vcc, s87, v6
	s_and_b64 s[40:41], s[66:67], vcc
	s_and_saveexec_b64 s[52:53], s[40:41]
	s_cbranch_execz .LBB0_1213
	v_mov_b32_e32 v7, s15
	v_cndmask_b32_e64 v7, v187, v7, s[2:3]
	v_lshlrev_b32_e32 v166, 8, v7
	v_lshl_add_u64 v[12:13], v[168:169], 0, v[166:167]
	v_mov_b32_e32 v16, v196
	v_mul_f32_e32 v8, v144, v200
	v_mul_f32_e32 v18, v140, v201
	v_mul_f32_e32 v12, v140, v200
	v_mov_b32_e32 v140, v145
	v_mul_f32_e32 v20, v144, v201
	v_mov_b32_e32 v144, v141
	v_pk_mul_f32 v[28:29], v[140:141], v[202:203]
	v_mov_b32_e32 v17, v198
	v_mov_b32_e32 v10, v197
	v_pk_mul_f32 v[14:15], v[144:145], v[202:203]
	v_mov_b32_e32 v9, v28
	v_mov_b32_e32 v19, v29
	v_mov_b32_e32 v11, v199
	v_pk_mul_f32 v[26:27], v[138:139], v[10:11]
	v_pk_mul_f32 v[10:11], v[142:143], v[10:11]
	v_mov_b32_e32 v13, v14
	v_mov_b32_e32 v21, v15
	v_pk_add_f32 v[8:9], v[8:9], v[18:19] neg_lo:[0,1] neg_hi:[0,1]
	v_pk_fma_f32 v[142:143], v[142:143], v[16:17], v[26:27] neg_lo:[0,0,1] neg_hi:[0,0,1]
	v_pk_fma_f32 v[138:139], v[138:139], v[16:17], v[10:11]
	v_pk_add_f32 v[140:141], v[12:13], v[20:21]
	v_mov_b32_e32 v144, v8
	v_mov_b32_e32 v145, v9
.LBB0_1213:
	s_or_b64 exec, exec, s[52:53]
	v_mov_b64_e32 v[8:9], s[4:5]
	v_mad_i64_i32 v[6:7], s[52:53], v6, s88, v[8:9]
	v_lshl_add_u64 v[6:7], v[22:23], 1, v[6:7]
	v_cvt_pk_bf16_f32 v8, v142, v143
	v_cvt_pk_bf16_f32 v9, v144, v145
	v_cvt_pk_bf16_f32 v10, v138, v139
	v_cvt_pk_bf16_f32 v11, v140, v141
	global_store_dwordx2 v[6:7], v[8:9], off
	global_store_dwordx2 v[6:7], v[10:11], off offset:32
	v_or_b32_e32 v8, 48, v24
	v_cmp_lt_i32_e32 vcc, s87, v8
	s_and_b64 s[52:53], s[66:67], vcc
	s_and_saveexec_b64 s[54:55], s[52:53]
	s_cbranch_execz .LBB0_1215
	v_mov_b32_e32 v9, s15
	v_cndmask_b32_e64 v9, v188, v9, s[2:3]
	v_lshlrev_b32_e32 v166, 8, v9
	v_lshl_add_u64 v[14:15], v[168:169], 0, v[166:167]
	v_mov_b32_e32 v18, v204
	v_mul_f32_e32 v10, v136, v208
	v_mul_f32_e32 v20, v132, v209
	v_mul_f32_e32 v14, v132, v208
	v_mov_b32_e32 v132, v137
	v_mul_f32_e32 v26, v136, v209
	v_mov_b32_e32 v136, v133
	v_pk_mul_f32 v[30:31], v[132:133], v[210:211]
	v_mov_b32_e32 v19, v206
	v_mov_b32_e32 v12, v205
	v_pk_mul_f32 v[16:17], v[136:137], v[210:211]
	v_mov_b32_e32 v11, v30
	v_mov_b32_e32 v21, v31
	v_mov_b32_e32 v13, v207
	v_pk_mul_f32 v[28:29], v[130:131], v[12:13]
	v_pk_mul_f32 v[12:13], v[134:135], v[12:13]
	v_mov_b32_e32 v15, v16
	v_mov_b32_e32 v27, v17
	v_pk_add_f32 v[10:11], v[10:11], v[20:21] neg_lo:[0,1] neg_hi:[0,1]
	v_pk_fma_f32 v[134:135], v[134:135], v[18:19], v[28:29] neg_lo:[0,0,1] neg_hi:[0,0,1]
	v_pk_fma_f32 v[130:131], v[130:131], v[18:19], v[12:13]
	v_pk_add_f32 v[132:133], v[14:15], v[26:27]
	v_mov_b32_e32 v136, v10
	v_mov_b32_e32 v137, v11
.LBB0_1215:
	s_or_b64 exec, exec, s[54:55]
	v_mov_b64_e32 v[10:11], s[4:5]
	v_mad_i64_i32 v[8:9], s[54:55], v8, s88, v[10:11]
	v_lshl_add_u64 v[8:9], v[22:23], 1, v[8:9]
	v_cvt_pk_bf16_f32 v10, v134, v135
	v_cvt_pk_bf16_f32 v11, v136, v137
	v_cvt_pk_bf16_f32 v12, v130, v131
	v_cvt_pk_bf16_f32 v13, v132, v133
	global_store_dwordx2 v[8:9], v[10:11], off
	global_store_dwordx2 v[8:9], v[12:13], off offset:32
	v_add_u32_e32 v10, 0x80, v24
	v_lshrrev_b32_e32 v11, 6, v10
	v_bitop3_b32 v18, v11, 16, 31 bitop3:0x6c
	v_cmp_lt_i32_e32 vcc, s89, v24
	v_cndmask_b32_e64 v11, v185, v18, s[2:3]
	s_and_b64 s[54:55], s[66:67], vcc
	v_lshlrev_b32_e32 v166, 8, v11
	s_and_saveexec_b64 s[56:57], s[54:55]
	s_cbranch_execz .LBB0_1217
	v_lshl_add_u64 v[16:17], v[168:169], 0, v[166:167]
	v_mov_b32_e32 v16, v212
	v_mul_f32_e32 v12, v128, v216
	v_mul_f32_e32 v20, v124, v217
	v_mul_f32_e32 v26, v124, v216
	v_mov_b32_e32 v124, v129
	v_mul_f32_e32 v30, v128, v217
	v_mov_b32_e32 v128, v125
	v_pk_mul_f32 v[124:125], v[124:125], v[218:219]
	v_mov_b32_e32 v17, v214
	v_mov_b32_e32 v14, v213
	v_pk_mul_f32 v[28:29], v[128:129], v[218:219]
	v_mov_b32_e32 v13, v124
	v_mov_b32_e32 v21, v125
	v_mov_b32_e32 v15, v215
	v_pk_mul_f32 v[32:33], v[122:123], v[14:15]
	v_pk_mul_f32 v[14:15], v[126:127], v[14:15]
	v_mov_b32_e32 v27, v28
	v_mov_b32_e32 v31, v29
	v_pk_add_f32 v[12:13], v[12:13], v[20:21] neg_lo:[0,1] neg_hi:[0,1]
	v_pk_fma_f32 v[126:127], v[126:127], v[16:17], v[32:33] neg_lo:[0,0,1] neg_hi:[0,0,1]
	v_pk_fma_f32 v[122:123], v[122:123], v[16:17], v[14:15]
	v_pk_add_f32 v[124:125], v[26:27], v[30:31]
	v_mov_b32_e32 v128, v12
	v_mov_b32_e32 v129, v13
; DI unsigned pk_bf16(float lo, float hi) { f32x2 v = {lo, hi}; hbf16x2 r = __builtin_convertvector(v, hbf16x2); return __builtin_bit_cast(unsigned, r); }
;     DI void operator()(const f32x4 (&acc)[2][2][4][2], const pg8::GU& u, int wr, int wc, int fr, int fq) const {
;     ...
;             const int col0 = 32 * g32 + 4 * fq;
; #pragma unroll
;             for (int ai = 0; ai < 2; ++ai)
; #pragma unroll
;                 for (int m = 0; m < 4; ++m) {
;                     const int row = row0 + ai * 128 + m * 16;
;                     f32x4 x1 = acc[ai][bj][m][0], x2 = acc[ai][bj][m][1];
;                     if (MODE == 0) { x1 *= 0.07216878364870322f * LOG2E; x2 *= 0.07216878364870322f * LOG2E; }
;                     if (rot && row >= NCTX) {
;                         const int t = (row - NCTX) & (SEQ - 1), pos = axis ? (t & 63) : (t >> 6);
;                         const f32x2* cs = R + pos * (MODE == 0 ? 16 : 32) + ibase;
;                         f32x4 o1, o2;
; #pragma unroll
;                         for (int j = 0; j < 4; ++j) { const f32x2 c = cs[j]; o1[j] = x1[j] * c[0] - x2[j] * c[1]; o2[j] = x2[j] * c[0] + x1[j] * c[1]; }
;                         x1 = o1; x2 = o2;
;                     }
;                     bf16_t* rowp = O + (size_t)row * ldc + col0;
;                     u32x2 w1, w2; w1.x = pk_bf16(x1[0], x1[1]); w1.y = pk_bf16(x1[2], x1[3]); w2.x = pk_bf16(x2[0], x2[1]); w2.y = pk_bf16(x2[2], x2[3]);
;                     *(u32x2*)(rowp) = w1; *(u32x2*)(rowp + 16) = w2;
;                 }
.LBB0_1217:
	s_or_b64 exec, exec, s[56:57]
	v_mov_b64_e32 v[12:13], s[4:5]
	v_mad_i64_i32 v[10:11], s[56:57], v10, s88, v[12:13]
	v_lshl_add_u64 v[12:13], v[22:23], 1, v[10:11]
	v_cvt_pk_bf16_f32 v10, v126, v127
	v_cvt_pk_bf16_f32 v11, v128, v129
	v_cvt_pk_bf16_f32 v14, v122, v123
	v_cvt_pk_bf16_f32 v15, v124, v125
	global_store_dwordx2 v[12:13], v[10:11], off
	global_store_dwordx2 v[12:13], v[14:15], off offset:32
	v_cmp_lt_i32_e32 vcc, s90, v24
	v_cndmask_b32_e64 v10, v186, v18, s[2:3]
	s_and_b64 s[56:57], s[66:67], vcc
	v_lshlrev_b32_e32 v10, 8, v10
	s_and_saveexec_b64 s[58:59], s[56:57]
	s_cbranch_execz .LBB0_1219
	v_mov_b32_e32 v11, v167
	v_lshl_add_u64 v[20:21], v[168:169], 0, v[10:11]
	v_mov_b32_e32 v20, v224
	v_mul_f32_e32 v14, v120, v228
	v_mul_f32_e32 v30, v116, v229
	v_mul_f32_e32 v26, v116, v228
	v_mov_b32_e32 v116, v121
	v_mul_f32_e32 v32, v120, v229
	v_mov_b32_e32 v120, v117
	v_pk_mul_f32 v[116:117], v[116:117], v[230:231]
	v_mov_b32_e32 v21, v226
	v_mov_b32_e32 v16, v225
	v_pk_mul_f32 v[28:29], v[120:121], v[230:231]
	v_mov_b32_e32 v15, v116
	v_mov_b32_e32 v31, v117
	v_mov_b32_e32 v17, v227
	v_pk_mul_f32 v[122:123], v[114:115], v[16:17]
	v_pk_mul_f32 v[16:17], v[118:119], v[16:17]
	v_mov_b32_e32 v27, v28
	v_mov_b32_e32 v33, v29
	v_pk_add_f32 v[14:15], v[14:15], v[30:31] neg_lo:[0,1] neg_hi:[0,1]
	v_pk_fma_f32 v[118:119], v[118:119], v[20:21], v[122:123] neg_lo:[0,0,1] neg_hi:[0,0,1]
	v_pk_fma_f32 v[114:115], v[114:115], v[20:21], v[16:17]
	v_pk_add_f32 v[116:117], v[26:27], v[32:33]
	v_mov_b32_e32 v120, v14
	v_mov_b32_e32 v121, v15
.LBB0_1219:
	s_or_b64 exec, exec, s[58:59]
	v_add_u32_e32 v11, 0x90, v24
	v_mov_b64_e32 v[14:15], s[4:5]
	v_mad_i64_i32 v[14:15], s[58:59], v11, s88, v[14:15]
	v_lshl_add_u64 v[16:17], v[22:23], 1, v[14:15]
	v_cvt_pk_bf16_f32 v14, v118, v119
	v_cvt_pk_bf16_f32 v15, v120, v121
	v_cmp_lt_i32_e32 vcc, s91, v24
	v_cndmask_b32_e64 v11, v187, v18, s[2:3]
	v_cvt_pk_bf16_f32 v20, v114, v115
	v_cvt_pk_bf16_f32 v21, v116, v117
	global_store_dwordx2 v[16:17], v[14:15], off
	global_store_dwordx2 v[16:17], v[20:21], off offset:32
	s_and_b64 s[58:59], s[66:67], vcc
	v_lshlrev_b32_e32 v14, 8, v11
	s_and_saveexec_b64 s[68:69], s[58:59]
	s_cbranch_execz .LBB0_1221
	v_mov_b32_e32 v15, v167
	v_lshl_add_u64 v[20:21], v[168:169], 0, v[14:15]
	v_mov_b32_e32 v20, v232
	v_mul_f32_e32 v26, v112, v236
	v_mul_f32_e32 v114, v108, v237
	v_mul_f32_e32 v30, v108, v236
	v_mov_b32_e32 v108, v113
	v_mov_b32_e32 v21, v234
	v_mov_b32_e32 v28, v233
	v_mul_f32_e32 v116, v112, v237
	v_mov_b32_e32 v112, v109
	v_pk_mul_f32 v[108:109], v[108:109], v[238:239]
	v_mov_b32_e32 v29, v235
	v_pk_mul_f32 v[118:119], v[106:107], v[28:29]
	v_pk_mul_f32 v[28:29], v[110:111], v[28:29]
	v_pk_mul_f32 v[32:33], v[112:113], v[238:239]
	v_mov_b32_e32 v27, v108
	v_mov_b32_e32 v115, v109
	v_pk_fma_f32 v[110:111], v[110:111], v[20:21], v[118:119] neg_lo:[0,0,1] neg_hi:[0,0,1]
	v_mov_b32_e32 v31, v32
	v_mov_b32_e32 v117, v33
	v_pk_fma_f32 v[106:107], v[106:107], v[20:21], v[28:29]
	v_pk_add_f32 v[20:21], v[26:27], v[114:115] neg_lo:[0,1] neg_hi:[0,1]
	v_pk_add_f32 v[108:109], v[30:31], v[116:117]
	v_mov_b32_e32 v112, v20
	v_mov_b32_e32 v113, v21
.LBB0_1221:
	s_or_b64 exec, exec, s[68:69]
	v_add_u32_e32 v11, 0xa0, v24
	v_mov_b64_e32 v[20:21], s[4:5]
	v_mad_i64_i32 v[20:21], s[68:69], v11, s88, v[20:21]
	v_cmp_lt_i32_e32 vcc, s92, v24
	v_cndmask_b32_e64 v11, v188, v18, s[2:3]
	v_lshl_add_u64 v[20:21], v[22:23], 1, v[20:21]
	v_cvt_pk_bf16_f32 v26, v110, v111
	v_cvt_pk_bf16_f32 v27, v112, v113
	s_and_b64 s[66:67], s[66:67], vcc
	v_lshlrev_b32_e32 v18, 8, v11
	v_cvt_pk_bf16_f32 v28, v106, v107
	v_cvt_pk_bf16_f32 v29, v108, v109
	global_store_dwordx2 v[20:21], v[26:27], off
	global_store_dwordx2 v[20:21], v[28:29], off offset:32
	s_and_saveexec_b64 s[68:69], s[66:67]
	s_cbranch_execz .LBB0_1223
	v_mov_b32_e32 v19, v167
	v_lshl_add_u64 v[30:31], v[168:169], 0, v[18:19]
	v_mov_b32_e32 v106, v240
	v_mul_f32_e32 v26, v104, v244
	v_mul_f32_e32 v108, v100, v245
	v_mul_f32_e32 v30, v100, v244
	v_mov_b32_e32 v100, v105
	v_mul_f32_e32 v110, v104, v245
	v_mov_b32_e32 v104, v101
	v_pk_mul_f32 v[100:101], v[100:101], v[246:247]
	v_mov_b32_e32 v107, v242
	v_mov_b32_e32 v28, v241
	v_pk_mul_f32 v[32:33], v[104:105], v[246:247]
	v_mov_b32_e32 v27, v100
	v_mov_b32_e32 v109, v101
	v_mov_b32_e32 v29, v243
	v_pk_mul_f32 v[112:113], v[98:99], v[28:29]
	v_pk_mul_f32 v[28:29], v[102:103], v[28:29]
	v_mov_b32_e32 v31, v32
	v_mov_b32_e32 v111, v33
	v_pk_add_f32 v[26:27], v[26:27], v[108:109] neg_lo:[0,1] neg_hi:[0,1]
	v_pk_fma_f32 v[102:103], v[102:103], v[106:107], v[112:113] neg_lo:[0,0,1] neg_hi:[0,0,1]
	v_pk_fma_f32 v[98:99], v[98:99], v[106:107], v[28:29]
	v_pk_add_f32 v[100:101], v[30:31], v[110:111]
	v_mov_b32_e32 v104, v26
	v_mov_b32_e32 v105, v27

; DI unsigned pk_bf16(float lo, float hi) { f32x2 v = {lo, hi}; hbf16x2 r = __builtin_convertvector(v, hbf16x2); return __builtin_bit_cast(unsigned, r); }
;     DI void operator()(const f32x4 (&acc)[2][2][4][2], const pg8::GU& u, int wr, int wc, int fr, int fq) const {
;         const int row0 = u.pm * 256 + wr * 64 + fr;
; #pragma unroll
;         for (int bj = 0; bj < 2; ++bj) {
;             const int g32 = 8 * u.pn + 4 * bj + wc;
;             int axis, ibase; bool rot;
;             if (MODE == 0) { const int hg = g32 % 6; rot = hg >= 4; axis = hg - 4; ibase = 4 * fq; }
;             else { rot = u.pn < 5; axis = (g32 & 3) >> 1; ibase = 16 * (g32 & 1) + 4 * fq; }
;             const int col0 = 32 * g32 + 4 * fq;
; #pragma unroll
;             for (int ai = 0; ai < 2; ++ai)
; #pragma unroll
;                 for (int m = 0; m < 4; ++m) {
;                     const int row = row0 + ai * 128 + m * 16;
;                     f32x4 x1 = acc[ai][bj][m][0], x2 = acc[ai][bj][m][1];
;                     if (MODE == 0) { x1 *= 0.07216878364870322f * LOG2E; x2 *= 0.07216878364870322f * LOG2E; }
;                     if (rot && row >= NCTX) {
;                         const int t = (row - NCTX) & (SEQ - 1), pos = axis ? (t & 63) : (t >> 6);
;                         const f32x2* cs = R + pos * (MODE == 0 ? 16 : 32) + ibase;
;                         f32x4 o1, o2;
; #pragma unroll
;                         for (int j = 0; j < 4; ++j) { const f32x2 c = cs[j]; o1[j] = x1[j] * c[0] - x2[j] * c[1]; o2[j] = x2[j] * c[0] + x1[j] * c[1]; }
;                         x1 = o1; x2 = o2;
;                     }
;                     bf16_t* rowp = O + (size_t)row * ldc + col0;
;                     u32x2 w1, w2; w1.x = pk_bf16(x1[0], x1[1]); w1.y = pk_bf16(x1[2], x1[3]); w2.x = pk_bf16(x2[0], x2[1]); w2.y = pk_bf16(x2[2], x2[3]);
;                     *(u32x2*)(rowp) = w1; *(u32x2*)(rowp + 16) = w2;
;                 }
.LBB0_1225:
	s_or_b64 exec, exec, s[68:69]
	v_cvt_pk_bf16_f32 v24, v94, v95
	v_cvt_pk_bf16_f32 v25, v96, v97
	v_cvt_pk_bf16_f32 v26, v90, v91
	v_cvt_pk_bf16_f32 v27, v92, v93
	global_store_dwordx2 v[2:3], v[24:25], off offset:256
	global_store_dwordx2 v[2:3], v[26:27], off offset:288
	s_and_saveexec_b64 s[34:35], s[30:31]
	s_cbranch_execz .LBB0_1227
	v_mov_b32_e32 v2, s15
	v_cndmask_b32_e64 v2, v186, v2, s[2:3]
	v_lshlrev_b32_e32 v2, 8, v2
	v_mov_b32_e32 v3, v167
	v_lshl_add_u64 v[2:3], v[168:169], 0, v[2:3]
	v_mov_b32_e32 v2, v176
	v_mul_f32_e32 v24, v88, v180
	v_mul_f32_e32 v32, v84, v181
	v_mul_f32_e32 v28, v84, v180
	v_mov_b32_e32 v84, v89
	v_mov_b32_e32 v3, v178
	v_mov_b32_e32 v26, v177
	v_mul_f32_e32 v90, v88, v181
	v_mov_b32_e32 v88, v85
	v_pk_mul_f32 v[84:85], v[84:85], v[182:183]
	v_mov_b32_e32 v27, v179
	v_pk_mul_f32 v[92:93], v[82:83], v[26:27]
	v_pk_mul_f32 v[26:27], v[86:87], v[26:27]
	v_pk_mul_f32 v[30:31], v[88:89], v[182:183]
	v_mov_b32_e32 v25, v84
	v_mov_b32_e32 v33, v85
	v_pk_fma_f32 v[86:87], v[86:87], v[2:3], v[92:93] neg_lo:[0,0,1] neg_hi:[0,0,1]
	v_mov_b32_e32 v29, v30
	v_mov_b32_e32 v91, v31
	v_pk_fma_f32 v[82:83], v[82:83], v[2:3], v[26:27]
	v_pk_add_f32 v[2:3], v[24:25], v[32:33] neg_lo:[0,1] neg_hi:[0,1]
	v_pk_add_f32 v[84:85], v[28:29], v[90:91]
	v_mov_b32_e32 v88, v2
	v_mov_b32_e32 v89, v3
.LBB0_1227:
	s_or_b64 exec, exec, s[34:35]
	v_cvt_pk_bf16_f32 v2, v86, v87
	v_cvt_pk_bf16_f32 v3, v88, v89
	v_cvt_pk_bf16_f32 v24, v82, v83
	v_cvt_pk_bf16_f32 v25, v84, v85
	global_store_dwordx2 v[4:5], v[2:3], off offset:256
	global_store_dwordx2 v[4:5], v[24:25], off offset:288
	s_and_saveexec_b64 s[30:31], s[40:41]
	s_cbranch_execz .LBB0_1229
	v_mov_b32_e32 v2, s15
	v_cndmask_b32_e64 v2, v187, v2, s[2:3]
	v_lshlrev_b32_e32 v2, 8, v2
	v_mov_b32_e32 v3, v167
	v_lshl_add_u64 v[24:25], v[168:169], 0, v[2:3]
	v_mov_b32_e32 v28, v196
	v_mul_f32_e32 v2, v80, v200
	v_mul_f32_e32 v30, v76, v201
	v_mul_f32_e32 v24, v76, v200
	v_mov_b32_e32 v76, v81
	v_mul_f32_e32 v32, v80, v201
	v_mov_b32_e32 v80, v77
	v_pk_mul_f32 v[76:77], v[76:77], v[202:203]
	v_mov_b32_e32 v29, v198
	v_mov_b32_e32 v4, v197
	v_pk_mul_f32 v[26:27], v[80:81], v[202:203]
	v_mov_b32_e32 v3, v76
	v_mov_b32_e32 v31, v77
	v_mov_b32_e32 v5, v199
	v_pk_mul_f32 v[82:83], v[74:75], v[4:5]
	v_pk_mul_f32 v[4:5], v[78:79], v[4:5]
	v_mov_b32_e32 v25, v26
	v_mov_b32_e32 v33, v27
	v_pk_add_f32 v[2:3], v[2:3], v[30:31] neg_lo:[0,1] neg_hi:[0,1]
	v_pk_fma_f32 v[78:79], v[78:79], v[28:29], v[82:83] neg_lo:[0,0,1] neg_hi:[0,0,1]
	v_pk_fma_f32 v[74:75], v[74:75], v[28:29], v[4:5]
	v_pk_add_f32 v[76:77], v[24:25], v[32:33]
	v_mov_b32_e32 v80, v2
	v_mov_b32_e32 v81, v3
.LBB0_1229:
	s_or_b64 exec, exec, s[30:31]
	v_cvt_pk_bf16_f32 v2, v78, v79
	v_cvt_pk_bf16_f32 v3, v80, v81
	v_cvt_pk_bf16_f32 v4, v74, v75
	v_cvt_pk_bf16_f32 v5, v76, v77
	global_store_dwordx2 v[6:7], v[2:3], off offset:256
	global_store_dwordx2 v[6:7], v[4:5], off offset:288
	s_and_saveexec_b64 s[30:31], s[52:53]
	s_cbranch_execz .LBB0_1231
	v_mov_b32_e32 v2, s15
	v_cndmask_b32_e64 v2, v188, v2, s[2:3]
	v_lshlrev_b32_e32 v2, 8, v2
	v_mov_b32_e32 v3, v167
	v_lshl_add_u64 v[6:7], v[168:169], 0, v[2:3]
	v_mov_b32_e32 v6, v204
	v_mul_f32_e32 v2, v72, v208
	v_mul_f32_e32 v28, v68, v209
	v_mul_f32_e32 v24, v68, v208
	v_mov_b32_e32 v68, v73
	v_mul_f32_e32 v30, v72, v209
	v_mov_b32_e32 v72, v69
	v_pk_mul_f32 v[68:69], v[68:69], v[210:211]
	v_mov_b32_e32 v7, v206
	v_mov_b32_e32 v4, v205
	v_pk_mul_f32 v[26:27], v[72:73], v[210:211]
	v_mov_b32_e32 v3, v68
	v_mov_b32_e32 v29, v69
	v_mov_b32_e32 v5, v207
	v_pk_mul_f32 v[32:33], v[66:67], v[4:5]
	v_pk_mul_f32 v[4:5], v[70:71], v[4:5]
	v_mov_b32_e32 v25, v26
	v_mov_b32_e32 v31, v27
	v_pk_add_f32 v[2:3], v[2:3], v[28:29] neg_lo:[0,1] neg_hi:[0,1]
	v_pk_fma_f32 v[70:71], v[70:71], v[6:7], v[32:33] neg_lo:[0,0,1] neg_hi:[0,0,1]
	v_pk_fma_f32 v[66:67], v[66:67], v[6:7], v[4:5]
	v_pk_add_f32 v[68:69], v[24:25], v[30:31]
	v_mov_b32_e32 v72, v2
	v_mov_b32_e32 v73, v3
; DI unsigned pk_bf16(float lo, float hi) { f32x2 v = {lo, hi}; hbf16x2 r = __builtin_convertvector(v, hbf16x2); return __builtin_bit_cast(unsigned, r); }
;     DI void operator()(const f32x4 (&acc)[2][2][4][2], const pg8::GU& u, int wr, int wc, int fr, int fq) const {
;         const int row0 = u.pm * 256 + wr * 64 + fr;
; #pragma unroll
;         for (int bj = 0; bj < 2; ++bj) {
;             const int g32 = 8 * u.pn + 4 * bj + wc;
;             int axis, ibase; bool rot;
;             if (MODE == 0) { const int hg = g32 % 6; rot = hg >= 4; axis = hg - 4; ibase = 4 * fq; }
;             else { rot = u.pn < 5; axis = (g32 & 3) >> 1; ibase = 16 * (g32 & 1) + 4 * fq; }
;             const int col0 = 32 * g32 + 4 * fq;
; #pragma unroll
;             for (int ai = 0; ai < 2; ++ai)
; #pragma unroll
;                 for (int m = 0; m < 4; ++m) {
;                     const int row = row0 + ai * 128 + m * 16;
;                     f32x4 x1 = acc[ai][bj][m][0], x2 = acc[ai][bj][m][1];
;                     if (MODE == 0) { x1 *= 0.07216878364870322f * LOG2E; x2 *= 0.07216878364870322f * LOG2E; }
;                     if (rot && row >= NCTX) {
;                         const int t = (row - NCTX) & (SEQ - 1), pos = axis ? (t & 63) : (t >> 6);
;                         const f32x2* cs = R + pos * (MODE == 0 ? 16 : 32) + ibase;
;                         f32x4 o1, o2;
; #pragma unroll
;                         for (int j = 0; j < 4; ++j) { const f32x2 c = cs[j]; o1[j] = x1[j] * c[0] - x2[j] * c[1]; o2[j] = x2[j] * c[0] + x1[j] * c[1]; }
;                         x1 = o1; x2 = o2;
;                     }
;                     bf16_t* rowp = O + (size_t)row * ldc + col0;
;                     u32x2 w1, w2; w1.x = pk_bf16(x1[0], x1[1]); w1.y = pk_bf16(x1[2], x1[3]); w2.x = pk_bf16(x2[0], x2[1]); w2.y = pk_bf16(x2[2], x2[3]);
;                     *(u32x2*)(rowp) = w1; *(u32x2*)(rowp + 16) = w2;
;                 }
.LBB0_1231:
	s_or_b64 exec, exec, s[30:31]
	v_cvt_pk_bf16_f32 v2, v70, v71
	v_cvt_pk_bf16_f32 v3, v72, v73
	v_cvt_pk_bf16_f32 v4, v66, v67
	v_cvt_pk_bf16_f32 v5, v68, v69
	global_store_dwordx2 v[8:9], v[2:3], off offset:256
	global_store_dwordx2 v[8:9], v[4:5], off offset:288
	s_and_saveexec_b64 s[30:31], s[54:55]
	s_cbranch_execz .LBB0_1233
	v_lshl_add_u64 v[6:7], v[168:169], 0, v[166:167]
	v_mov_b32_e32 v24, v212
	v_mul_f32_e32 v2, v64, v216
	v_mul_f32_e32 v26, v60, v217
	v_mul_f32_e32 v6, v60, v216
	v_mov_b32_e32 v60, v65
	v_mul_f32_e32 v28, v64, v217
	v_mov_b32_e32 v64, v61
	v_pk_mul_f32 v[32:33], v[60:61], v[218:219]
	v_mov_b32_e32 v25, v214
	v_mov_b32_e32 v4, v213
	v_pk_mul_f32 v[8:9], v[64:65], v[218:219]
	v_mov_b32_e32 v3, v32
	v_mov_b32_e32 v27, v33
	v_mov_b32_e32 v5, v215
	v_pk_mul_f32 v[30:31], v[58:59], v[4:5]
	v_pk_mul_f32 v[4:5], v[62:63], v[4:5]
	v_mov_b32_e32 v7, v8
	v_mov_b32_e32 v29, v9
	v_pk_add_f32 v[2:3], v[2:3], v[26:27] neg_lo:[0,1] neg_hi:[0,1]
	v_pk_fma_f32 v[62:63], v[62:63], v[24:25], v[30:31] neg_lo:[0,0,1] neg_hi:[0,0,1]
	v_pk_fma_f32 v[58:59], v[58:59], v[24:25], v[4:5]
	v_pk_add_f32 v[60:61], v[6:7], v[28:29]
	v_mov_b32_e32 v64, v2
	v_mov_b32_e32 v65, v3
.LBB0_1233:
	s_or_b64 exec, exec, s[30:31]
	v_cvt_pk_bf16_f32 v2, v62, v63
	v_cvt_pk_bf16_f32 v3, v64, v65
	v_cvt_pk_bf16_f32 v4, v58, v59
	v_cvt_pk_bf16_f32 v5, v60, v61
	global_store_dwordx2 v[12:13], v[2:3], off offset:256
	global_store_dwordx2 v[12:13], v[4:5], off offset:288
	s_and_saveexec_b64 s[30:31], s[56:57]
	s_cbranch_execz .LBB0_1235
	v_mov_b32_e32 v11, v167
	v_lshl_add_u64 v[6:7], v[168:169], 0, v[10:11]
	v_mov_b32_e32 v10, v224
	v_mul_f32_e32 v2, v56, v228
	v_mul_f32_e32 v12, v52, v229
	v_mul_f32_e32 v6, v52, v228
	v_mov_b32_e32 v52, v57
	v_mul_f32_e32 v24, v56, v229
	v_mov_b32_e32 v56, v53
	v_pk_mul_f32 v[28:29], v[52:53], v[230:231]
	v_mov_b32_e32 v11, v226
	v_mov_b32_e32 v4, v225
	v_pk_mul_f32 v[8:9], v[56:57], v[230:231]
	v_mov_b32_e32 v3, v28
	v_mov_b32_e32 v13, v29
	v_mov_b32_e32 v5, v227
	v_pk_mul_f32 v[26:27], v[50:51], v[4:5]
	v_pk_mul_f32 v[4:5], v[54:55], v[4:5]
	v_mov_b32_e32 v7, v8
	v_mov_b32_e32 v25, v9
	v_pk_add_f32 v[2:3], v[2:3], v[12:13] neg_lo:[0,1] neg_hi:[0,1]
	v_pk_fma_f32 v[54:55], v[54:55], v[10:11], v[26:27] neg_lo:[0,0,1] neg_hi:[0,0,1]
	v_pk_fma_f32 v[50:51], v[50:51], v[10:11], v[4:5]
	v_pk_add_f32 v[52:53], v[6:7], v[24:25]
	v_mov_b32_e32 v56, v2
	v_mov_b32_e32 v57, v3
.LBB0_1235:
	s_or_b64 exec, exec, s[30:31]
	v_cvt_pk_bf16_f32 v2, v54, v55
	v_cvt_pk_bf16_f32 v3, v56, v57
	v_cvt_pk_bf16_f32 v4, v50, v51
	v_cvt_pk_bf16_f32 v5, v52, v53
	global_store_dwordx2 v[16:17], v[2:3], off offset:256
	global_store_dwordx2 v[16:17], v[4:5], off offset:288
	s_and_saveexec_b64 s[30:31], s[58:59]
	s_cbranch_execz .LBB0_1237
	v_mov_b32_e32 v15, v167
	v_lshl_add_u64 v[6:7], v[168:169], 0, v[14:15]
	v_mov_b32_e32 v10, v232
	v_mul_f32_e32 v2, v48, v236
	v_mul_f32_e32 v12, v44, v237
	v_mul_f32_e32 v6, v44, v236
	v_mov_b32_e32 v44, v49
	v_mul_f32_e32 v14, v48, v237
	v_mov_b32_e32 v48, v45
	v_pk_mul_f32 v[24:25], v[44:45], v[238:239]
	v_mov_b32_e32 v11, v234
	v_mov_b32_e32 v4, v233
	v_pk_mul_f32 v[8:9], v[48:49], v[238:239]
	v_mov_b32_e32 v3, v24
	v_mov_b32_e32 v13, v25
	v_mov_b32_e32 v5, v235
	v_pk_mul_f32 v[16:17], v[42:43], v[4:5]
	v_pk_mul_f32 v[4:5], v[46:47], v[4:5]
	v_mov_b32_e32 v7, v8
	v_mov_b32_e32 v15, v9
	v_pk_add_f32 v[2:3], v[2:3], v[12:13] neg_lo:[0,1] neg_hi:[0,1]
	v_pk_fma_f32 v[46:47], v[46:47], v[10:11], v[16:17] neg_lo:[0,0,1] neg_hi:[0,0,1]
	v_pk_fma_f32 v[42:43], v[42:43], v[10:11], v[4:5]
	v_pk_add_f32 v[44:45], v[6:7], v[14:15]
	v_mov_b32_e32 v48, v2
	v_mov_b32_e32 v49, v3
.LBB0_1237:
	s_or_b64 exec, exec, s[30:31]
	v_cvt_pk_bf16_f32 v2, v46, v47
	v_cvt_pk_bf16_f32 v3, v48, v49
	v_cvt_pk_bf16_f32 v4, v42, v43
	v_cvt_pk_bf16_f32 v5, v44, v45
	global_store_dwordx2 v[20:21], v[2:3], off offset:256
	global_store_dwordx2 v[20:21], v[4:5], off offset:288
	s_and_saveexec_b64 s[30:31], s[66:67]
	s_cbranch_execz .LBB0_1239
	v_mov_b32_e32 v19, v167
	v_lshl_add_u64 v[6:7], v[168:169], 0, v[18:19]
	v_mov_b32_e32 v10, v240
	v_mul_f32_e32 v2, v40, v244
	v_mul_f32_e32 v12, v36, v245
	v_mul_f32_e32 v6, v36, v244
	v_mov_b32_e32 v36, v41
	v_mul_f32_e32 v14, v40, v245
	v_mov_b32_e32 v40, v37
	v_pk_mul_f32 v[18:19], v[36:37], v[246:247]
	v_mov_b32_e32 v11, v242
	v_mov_b32_e32 v4, v241
	v_pk_mul_f32 v[8:9], v[40:41], v[246:247]
	v_mov_b32_e32 v3, v18
	v_mov_b32_e32 v13, v19
	v_mov_b32_e32 v5, v243
	v_pk_mul_f32 v[16:17], v[34:35], v[4:5]
	v_pk_mul_f32 v[4:5], v[38:39], v[4:5]
	v_mov_b32_e32 v7, v8
	v_mov_b32_e32 v15, v9
	v_pk_add_f32 v[2:3], v[2:3], v[12:13] neg_lo:[0,1] neg_hi:[0,1]
	v_pk_fma_f32 v[38:39], v[38:39], v[10:11], v[16:17] neg_lo:[0,0,1] neg_hi:[0,0,1]
	v_pk_fma_f32 v[34:35], v[34:35], v[10:11], v[4:5]
	v_pk_add_f32 v[36:37], v[6:7], v[14:15]
	v_mov_b32_e32 v40, v2
	v_mov_b32_e32 v41, v3
